# router LDS reads: read-ahead depth 4 instead of 3 (six rotating quads), otherwise v86
# speedup vs baseline: 1.0144x; 1.0144x over previous
; #define LAS __attribute__((address_space(3)))
; __device__ __forceinline__ void phase_norm2(const Params& p, const Ctx& F, const int l) {
;     ...
;         f32x2 lg[16];
;         unsigned wro = (unsigned)(uintptr_t)wr; asm volatile("" : "+v"(wro));
;         const LAS float* wr2 = (const LAS float*)(uintptr_t)wro;
; #pragma unroll
;         for (int e = 0; e < 16; ++e) { f32x2 a = {0.f, 0.f};
; #pragma unroll
;             for (int j = 0; j < 8; ++j) { const f32x4 w = *((const LAS f32x4*)(wr2 + e * DM) + F.lane + 64 * j);
; #pragma unroll
;                 for (int c = 0; c < 4; ++c) a += vv[j][c] * w[c]; }
;             lg[e] = a; }
.LBB0_937:
	s_or_b64 exec, exec, s[12:13]
	v_mov_b32_e32 v1, v35
	s_nop 0
	v_lshl_add_u32 v182, v132, 4, v1
	v_add_u32_e32 v202, 0x10000, v182
	ds_read_b128 v[224:227], v182
	ds_read_b128 v[228:231], v182 offset:1024
	ds_read_b128 v[232:235], v182 offset:2048
	ds_read_b128 v[236:239], v182 offset:3072
	ds_read_b128 v[240:243], v182 offset:4096
	s_waitcnt lgkmcnt(4)
	v_pk_fma_f32 v[156:157], v[124:125], v[224:225], 0 op_sel_hi:[1,0,0]
	s_nop 0
	v_pk_fma_f32 v[152:153], v[126:127], v[224:225], v[156:157] op_sel:[0,1,0]
	s_nop 0
	v_pk_fma_f32 v[152:153], v[128:129], v[226:227], v[152:153] op_sel_hi:[1,0,1]
	v_mov_b32_e32 v154, v227
	v_pk_fma_f32 v[156:157], v[130:131], v[154:155], v[152:153] op_sel_hi:[1,0,1]
	ds_read_b128 v[244:247], v182 offset:5120
	s_waitcnt lgkmcnt(4)
	v_pk_fma_f32 v[156:157], v[112:113], v[228:229], v[156:157] op_sel_hi:[1,0,1]
	s_nop 0
	v_pk_fma_f32 v[152:153], v[114:115], v[228:229], v[156:157] op_sel:[0,1,0]
	s_nop 0
	v_pk_fma_f32 v[152:153], v[118:119], v[230:231], v[152:153] op_sel_hi:[1,0,1]
	v_mov_b32_e32 v154, v231
	v_pk_fma_f32 v[156:157], v[122:123], v[154:155], v[152:153] op_sel_hi:[1,0,1]
	ds_read_b128 v[224:227], v182 offset:6144
	s_waitcnt lgkmcnt(4)
	v_pk_fma_f32 v[156:157], v[108:109], v[232:233], v[156:157] op_sel_hi:[1,0,1]
	s_nop 0
	v_pk_fma_f32 v[152:153], v[110:111], v[232:233], v[156:157] op_sel:[0,1,0]
	s_nop 0
	v_pk_fma_f32 v[152:153], v[116:117], v[234:235], v[152:153] op_sel_hi:[1,0,1]
	v_mov_b32_e32 v154, v235
	v_pk_fma_f32 v[156:157], v[120:121], v[154:155], v[152:153] op_sel_hi:[1,0,1]
	ds_read_b128 v[228:231], v182 offset:7168
	s_waitcnt lgkmcnt(4)
	v_pk_fma_f32 v[156:157], v[96:97], v[236:237], v[156:157] op_sel_hi:[1,0,1]
	s_nop 0
	v_pk_fma_f32 v[152:153], v[98:99], v[236:237], v[156:157] op_sel:[0,1,0]
	s_nop 0
	v_pk_fma_f32 v[152:153], v[102:103], v[238:239], v[152:153] op_sel_hi:[1,0,1]
	v_mov_b32_e32 v154, v239
	v_pk_fma_f32 v[156:157], v[106:107], v[154:155], v[152:153] op_sel_hi:[1,0,1]
	ds_read_b128 v[232:235], v182 offset:8192
	s_waitcnt lgkmcnt(4)
	v_pk_fma_f32 v[156:157], v[92:93], v[240:241], v[156:157] op_sel_hi:[1,0,1]
	s_nop 0
	v_pk_fma_f32 v[152:153], v[94:95], v[240:241], v[156:157] op_sel:[0,1,0]
	s_nop 0
	v_pk_fma_f32 v[152:153], v[100:101], v[242:243], v[152:153] op_sel_hi:[1,0,1]
	v_mov_b32_e32 v154, v243
	v_pk_fma_f32 v[156:157], v[104:105], v[154:155], v[152:153] op_sel_hi:[1,0,1]
	ds_read_b128 v[236:239], v182 offset:9216
	s_waitcnt lgkmcnt(4)
	v_pk_fma_f32 v[156:157], v[80:81], v[244:245], v[156:157] op_sel_hi:[1,0,1]
	s_nop 0
	v_pk_fma_f32 v[152:153], v[82:83], v[244:245], v[156:157] op_sel:[0,1,0]
	s_nop 0
	v_pk_fma_f32 v[152:153], v[86:87], v[246:247], v[152:153] op_sel_hi:[1,0,1]
	v_mov_b32_e32 v154, v247
	v_pk_fma_f32 v[156:157], v[90:91], v[154:155], v[152:153] op_sel_hi:[1,0,1]
	ds_read_b128 v[240:243], v182 offset:10240
	s_waitcnt lgkmcnt(4)
	v_pk_fma_f32 v[156:157], v[76:77], v[224:225], v[156:157] op_sel_hi:[1,0,1]
	s_nop 0
	v_pk_fma_f32 v[152:153], v[78:79], v[224:225], v[156:157] op_sel:[0,1,0]
	s_nop 0
	v_pk_fma_f32 v[152:153], v[84:85], v[226:227], v[152:153] op_sel_hi:[1,0,1]
	v_mov_b32_e32 v154, v227
	v_pk_fma_f32 v[156:157], v[88:89], v[154:155], v[152:153] op_sel_hi:[1,0,1]
	ds_read_b128 v[244:247], v182 offset:11264
	s_waitcnt lgkmcnt(4)
	v_pk_fma_f32 v[156:157], v[68:69], v[228:229], v[156:157] op_sel_hi:[1,0,1]
	s_nop 0
	v_pk_fma_f32 v[152:153], v[70:71], v[228:229], v[156:157] op_sel:[0,1,0]
	s_nop 0
	v_pk_fma_f32 v[152:153], v[72:73], v[230:231], v[152:153] op_sel_hi:[1,0,1]
	v_mov_b32_e32 v154, v231
	v_pk_fma_f32 v[152:153], v[74:75], v[154:155], v[152:153] op_sel_hi:[1,0,1]
	ds_read_b128 v[224:227], v182 offset:12288
	s_waitcnt lgkmcnt(4)
	v_pk_fma_f32 v[158:159], v[124:125], v[232:233], 0 op_sel_hi:[1,0,0]
	s_nop 0
	v_pk_fma_f32 v[154:155], v[126:127], v[232:233], v[158:159] op_sel:[0,1,0]
	s_nop 0
	v_pk_fma_f32 v[154:155], v[128:129], v[234:235], v[154:155] op_sel_hi:[1,0,1]
	v_mov_b32_e32 v156, v235
	v_pk_fma_f32 v[158:159], v[130:131], v[156:157], v[154:155] op_sel_hi:[1,0,1]
	ds_read_b128 v[228:231], v182 offset:13312
	s_waitcnt lgkmcnt(4)
	v_pk_fma_f32 v[158:159], v[112:113], v[236:237], v[158:159] op_sel_hi:[1,0,1]
	s_nop 0
	v_pk_fma_f32 v[154:155], v[114:115], v[236:237], v[158:159] op_sel:[0,1,0]
	s_nop 0
	v_pk_fma_f32 v[154:155], v[118:119], v[238:239], v[154:155] op_sel_hi:[1,0,1]
	v_mov_b32_e32 v156, v239
	v_pk_fma_f32 v[158:159], v[122:123], v[156:157], v[154:155] op_sel_hi:[1,0,1]
	ds_read_b128 v[232:235], v182 offset:14336
	s_waitcnt lgkmcnt(4)
	v_pk_fma_f32 v[158:159], v[108:109], v[240:241], v[158:159] op_sel_hi:[1,0,1]
	s_nop 0
	v_pk_fma_f32 v[154:155], v[110:111], v[240:241], v[158:159] op_sel:[0,1,0]
	s_nop 0
	v_pk_fma_f32 v[154:155], v[116:117], v[242:243], v[154:155] op_sel_hi:[1,0,1]
	v_mov_b32_e32 v156, v243
	v_pk_fma_f32 v[158:159], v[120:121], v[156:157], v[154:155] op_sel_hi:[1,0,1]
	ds_read_b128 v[236:239], v182 offset:15360
	s_waitcnt lgkmcnt(4)
	v_pk_fma_f32 v[158:159], v[96:97], v[244:245], v[158:159] op_sel_hi:[1,0,1]
	s_nop 0
	v_pk_fma_f32 v[154:155], v[98:99], v[244:245], v[158:159] op_sel:[0,1,0]
	s_nop 0
	v_pk_fma_f32 v[154:155], v[102:103], v[246:247], v[154:155] op_sel_hi:[1,0,1]
	v_mov_b32_e32 v156, v247
	v_pk_fma_f32 v[158:159], v[106:107], v[156:157], v[154:155] op_sel_hi:[1,0,1]
	ds_read_b128 v[240:243], v182 offset:16384
	s_waitcnt lgkmcnt(4)
	v_pk_fma_f32 v[158:159], v[92:93], v[224:225], v[158:159] op_sel_hi:[1,0,1]
	s_nop 0
	v_pk_fma_f32 v[154:155], v[94:95], v[224:225], v[158:159] op_sel:[0,1,0]
	s_nop 0
	v_pk_fma_f32 v[154:155], v[100:101], v[226:227], v[154:155] op_sel_hi:[1,0,1]
	v_mov_b32_e32 v156, v227
	v_pk_fma_f32 v[158:159], v[104:105], v[156:157], v[154:155] op_sel_hi:[1,0,1]
	ds_read_b128 v[244:247], v182 offset:17408
	s_waitcnt lgkmcnt(4)
; #define LAS __attribute__((address_space(3)))
; __device__ __forceinline__ void phase_norm2(const Params& p, const Ctx& F, const int l) {
;     ...
; #pragma unroll
;         for (int e = 0; e < 16; ++e) { f32x2 a = {0.f, 0.f};
; #pragma unroll
;             for (int j = 0; j < 8; ++j) { const f32x4 w = *((const LAS f32x4*)(wr2 + e * DM) + F.lane + 64 * j);
; #pragma unroll
;                 for (int c = 0; c < 4; ++c) a += vv[j][c] * w[c]; }
;             lg[e] = a; }
	v_pk_fma_f32 v[158:159], v[80:81], v[228:229], v[158:159] op_sel_hi:[1,0,1]
	s_nop 0
	v_pk_fma_f32 v[154:155], v[82:83], v[228:229], v[158:159] op_sel:[0,1,0]
	s_nop 0
	v_pk_fma_f32 v[154:155], v[86:87], v[230:231], v[154:155] op_sel_hi:[1,0,1]
	v_mov_b32_e32 v156, v231
	v_pk_fma_f32 v[158:159], v[90:91], v[156:157], v[154:155] op_sel_hi:[1,0,1]
	ds_read_b128 v[224:227], v182 offset:18432
	s_waitcnt lgkmcnt(4)
	v_pk_fma_f32 v[158:159], v[76:77], v[232:233], v[158:159] op_sel_hi:[1,0,1]
	s_nop 0
	v_pk_fma_f32 v[154:155], v[78:79], v[232:233], v[158:159] op_sel:[0,1,0]
	s_nop 0
	v_pk_fma_f32 v[154:155], v[84:85], v[234:235], v[154:155] op_sel_hi:[1,0,1]
	v_mov_b32_e32 v156, v235
	v_pk_fma_f32 v[158:159], v[88:89], v[156:157], v[154:155] op_sel_hi:[1,0,1]
	ds_read_b128 v[228:231], v182 offset:19456
	s_waitcnt lgkmcnt(4)
	v_pk_fma_f32 v[158:159], v[68:69], v[236:237], v[158:159] op_sel_hi:[1,0,1]
	s_nop 0
	v_pk_fma_f32 v[154:155], v[70:71], v[236:237], v[158:159] op_sel:[0,1,0]
	s_nop 0
	v_pk_fma_f32 v[154:155], v[72:73], v[238:239], v[154:155] op_sel_hi:[1,0,1]
	v_mov_b32_e32 v156, v239
	v_pk_fma_f32 v[154:155], v[74:75], v[156:157], v[154:155] op_sel_hi:[1,0,1]
	ds_read_b128 v[232:235], v182 offset:20480
	s_waitcnt lgkmcnt(4)
	v_pk_fma_f32 v[160:161], v[124:125], v[240:241], 0 op_sel_hi:[1,0,0]
	s_nop 0
	v_pk_fma_f32 v[156:157], v[126:127], v[240:241], v[160:161] op_sel:[0,1,0]
	s_nop 0
	v_pk_fma_f32 v[156:157], v[128:129], v[242:243], v[156:157] op_sel_hi:[1,0,1]
	v_mov_b32_e32 v158, v243
	v_pk_fma_f32 v[160:161], v[130:131], v[158:159], v[156:157] op_sel_hi:[1,0,1]
	ds_read_b128 v[236:239], v182 offset:21504
	s_waitcnt lgkmcnt(4)
	v_pk_fma_f32 v[160:161], v[112:113], v[244:245], v[160:161] op_sel_hi:[1,0,1]
	s_nop 0
	v_pk_fma_f32 v[156:157], v[114:115], v[244:245], v[160:161] op_sel:[0,1,0]
	s_nop 0
	v_pk_fma_f32 v[156:157], v[118:119], v[246:247], v[156:157] op_sel_hi:[1,0,1]
	v_mov_b32_e32 v158, v247
	v_pk_fma_f32 v[160:161], v[122:123], v[158:159], v[156:157] op_sel_hi:[1,0,1]
	ds_read_b128 v[240:243], v182 offset:22528
	s_waitcnt lgkmcnt(4)
	v_pk_fma_f32 v[160:161], v[108:109], v[224:225], v[160:161] op_sel_hi:[1,0,1]
	s_nop 0
	v_pk_fma_f32 v[156:157], v[110:111], v[224:225], v[160:161] op_sel:[0,1,0]
	s_nop 0
	v_pk_fma_f32 v[156:157], v[116:117], v[226:227], v[156:157] op_sel_hi:[1,0,1]
	v_mov_b32_e32 v158, v227
	v_pk_fma_f32 v[160:161], v[120:121], v[158:159], v[156:157] op_sel_hi:[1,0,1]
	ds_read_b128 v[244:247], v182 offset:23552
	s_waitcnt lgkmcnt(4)
	v_pk_fma_f32 v[160:161], v[96:97], v[228:229], v[160:161] op_sel_hi:[1,0,1]
	s_nop 0
	v_pk_fma_f32 v[156:157], v[98:99], v[228:229], v[160:161] op_sel:[0,1,0]
	s_nop 0
	v_pk_fma_f32 v[156:157], v[102:103], v[230:231], v[156:157] op_sel_hi:[1,0,1]
	v_mov_b32_e32 v158, v231
	v_pk_fma_f32 v[160:161], v[106:107], v[158:159], v[156:157] op_sel_hi:[1,0,1]
	ds_read_b128 v[224:227], v182 offset:24576
	s_waitcnt lgkmcnt(4)
	v_pk_fma_f32 v[160:161], v[92:93], v[232:233], v[160:161] op_sel_hi:[1,0,1]
	s_nop 0
	v_pk_fma_f32 v[156:157], v[94:95], v[232:233], v[160:161] op_sel:[0,1,0]
	s_nop 0
	v_pk_fma_f32 v[156:157], v[100:101], v[234:235], v[156:157] op_sel_hi:[1,0,1]
	v_mov_b32_e32 v158, v235
	v_pk_fma_f32 v[160:161], v[104:105], v[158:159], v[156:157] op_sel_hi:[1,0,1]
	ds_read_b128 v[228:231], v182 offset:25600
	s_waitcnt lgkmcnt(4)
	v_pk_fma_f32 v[160:161], v[80:81], v[236:237], v[160:161] op_sel_hi:[1,0,1]
	s_nop 0
	v_pk_fma_f32 v[156:157], v[82:83], v[236:237], v[160:161] op_sel:[0,1,0]
	s_nop 0
	v_pk_fma_f32 v[156:157], v[86:87], v[238:239], v[156:157] op_sel_hi:[1,0,1]
	v_mov_b32_e32 v158, v239
	v_pk_fma_f32 v[160:161], v[90:91], v[158:159], v[156:157] op_sel_hi:[1,0,1]
	ds_read_b128 v[232:235], v182 offset:26624
	s_waitcnt lgkmcnt(4)
	v_pk_fma_f32 v[160:161], v[76:77], v[240:241], v[160:161] op_sel_hi:[1,0,1]
	s_nop 0
	v_pk_fma_f32 v[156:157], v[78:79], v[240:241], v[160:161] op_sel:[0,1,0]
	s_nop 0
	v_pk_fma_f32 v[156:157], v[84:85], v[242:243], v[156:157] op_sel_hi:[1,0,1]
	v_mov_b32_e32 v158, v243
	v_pk_fma_f32 v[160:161], v[88:89], v[158:159], v[156:157] op_sel_hi:[1,0,1]
	ds_read_b128 v[236:239], v182 offset:27648
	s_waitcnt lgkmcnt(4)
	v_pk_fma_f32 v[160:161], v[68:69], v[244:245], v[160:161] op_sel_hi:[1,0,1]
	s_nop 0
	v_pk_fma_f32 v[156:157], v[70:71], v[244:245], v[160:161] op_sel:[0,1,0]
	s_nop 0
	v_pk_fma_f32 v[156:157], v[72:73], v[246:247], v[156:157] op_sel_hi:[1,0,1]
	v_mov_b32_e32 v158, v247
	v_pk_fma_f32 v[156:157], v[74:75], v[158:159], v[156:157] op_sel_hi:[1,0,1]
	ds_read_b128 v[240:243], v182 offset:28672
	s_waitcnt lgkmcnt(4)
	v_pk_fma_f32 v[162:163], v[124:125], v[224:225], 0 op_sel_hi:[1,0,0]
	s_nop 0
	v_pk_fma_f32 v[158:159], v[126:127], v[224:225], v[162:163] op_sel:[0,1,0]
	s_nop 0
	v_pk_fma_f32 v[158:159], v[128:129], v[226:227], v[158:159] op_sel_hi:[1,0,1]
	v_mov_b32_e32 v160, v227
	v_pk_fma_f32 v[162:163], v[130:131], v[160:161], v[158:159] op_sel_hi:[1,0,1]
	ds_read_b128 v[244:247], v182 offset:29696
	s_waitcnt lgkmcnt(4)
	v_pk_fma_f32 v[162:163], v[112:113], v[228:229], v[162:163] op_sel_hi:[1,0,1]
	s_nop 0
	v_pk_fma_f32 v[158:159], v[114:115], v[228:229], v[162:163] op_sel:[0,1,0]
	s_nop 0
	v_pk_fma_f32 v[158:159], v[118:119], v[230:231], v[158:159] op_sel_hi:[1,0,1]
	v_mov_b32_e32 v160, v231
	v_pk_fma_f32 v[162:163], v[122:123], v[160:161], v[158:159] op_sel_hi:[1,0,1]
	ds_read_b128 v[224:227], v182 offset:30720
	s_waitcnt lgkmcnt(4)
	v_pk_fma_f32 v[162:163], v[108:109], v[232:233], v[162:163] op_sel_hi:[1,0,1]
	s_nop 0
	v_pk_fma_f32 v[158:159], v[110:111], v[232:233], v[162:163] op_sel:[0,1,0]
	s_nop 0
	v_pk_fma_f32 v[158:159], v[116:117], v[234:235], v[158:159] op_sel_hi:[1,0,1]
	v_mov_b32_e32 v160, v235
	v_pk_fma_f32 v[162:163], v[120:121], v[160:161], v[158:159] op_sel_hi:[1,0,1]
	ds_read_b128 v[228:231], v182 offset:31744
	s_waitcnt lgkmcnt(4)
; #define LAS __attribute__((address_space(3)))
; __device__ __forceinline__ void phase_norm2(const Params& p, const Ctx& F, const int l) {
;     ...
; #pragma unroll
;         for (int e = 0; e < 16; ++e) { f32x2 a = {0.f, 0.f};
; #pragma unroll
;             for (int j = 0; j < 8; ++j) { const f32x4 w = *((const LAS f32x4*)(wr2 + e * DM) + F.lane + 64 * j);
; #pragma unroll
;                 for (int c = 0; c < 4; ++c) a += vv[j][c] * w[c]; }
;             lg[e] = a; }
	v_pk_fma_f32 v[162:163], v[96:97], v[236:237], v[162:163] op_sel_hi:[1,0,1]
	s_nop 0
	v_pk_fma_f32 v[158:159], v[98:99], v[236:237], v[162:163] op_sel:[0,1,0]
	s_nop 0
	v_pk_fma_f32 v[158:159], v[102:103], v[238:239], v[158:159] op_sel_hi:[1,0,1]
	v_mov_b32_e32 v160, v239
	v_pk_fma_f32 v[162:163], v[106:107], v[160:161], v[158:159] op_sel_hi:[1,0,1]
	ds_read_b128 v[232:235], v182 offset:32768
	s_waitcnt lgkmcnt(4)
	v_pk_fma_f32 v[162:163], v[92:93], v[240:241], v[162:163] op_sel_hi:[1,0,1]
	s_nop 0
	v_pk_fma_f32 v[158:159], v[94:95], v[240:241], v[162:163] op_sel:[0,1,0]
	s_nop 0
	v_pk_fma_f32 v[158:159], v[100:101], v[242:243], v[158:159] op_sel_hi:[1,0,1]
	v_mov_b32_e32 v160, v243
	v_pk_fma_f32 v[162:163], v[104:105], v[160:161], v[158:159] op_sel_hi:[1,0,1]
	ds_read_b128 v[236:239], v182 offset:33792
	s_waitcnt lgkmcnt(4)
	v_pk_fma_f32 v[162:163], v[80:81], v[244:245], v[162:163] op_sel_hi:[1,0,1]
	s_nop 0
	v_pk_fma_f32 v[158:159], v[82:83], v[244:245], v[162:163] op_sel:[0,1,0]
	s_nop 0
	v_pk_fma_f32 v[158:159], v[86:87], v[246:247], v[158:159] op_sel_hi:[1,0,1]
	v_mov_b32_e32 v160, v247
	v_pk_fma_f32 v[162:163], v[90:91], v[160:161], v[158:159] op_sel_hi:[1,0,1]
	ds_read_b128 v[240:243], v182 offset:34816
	s_waitcnt lgkmcnt(4)
	v_pk_fma_f32 v[162:163], v[76:77], v[224:225], v[162:163] op_sel_hi:[1,0,1]
	s_nop 0
	v_pk_fma_f32 v[158:159], v[78:79], v[224:225], v[162:163] op_sel:[0,1,0]
	s_nop 0
	v_pk_fma_f32 v[158:159], v[84:85], v[226:227], v[158:159] op_sel_hi:[1,0,1]
	v_mov_b32_e32 v160, v227
	v_pk_fma_f32 v[162:163], v[88:89], v[160:161], v[158:159] op_sel_hi:[1,0,1]
	ds_read_b128 v[244:247], v182 offset:35840
	s_waitcnt lgkmcnt(4)
	v_pk_fma_f32 v[162:163], v[68:69], v[228:229], v[162:163] op_sel_hi:[1,0,1]
	s_nop 0
	v_pk_fma_f32 v[158:159], v[70:71], v[228:229], v[162:163] op_sel:[0,1,0]
	s_nop 0
	v_pk_fma_f32 v[158:159], v[72:73], v[230:231], v[158:159] op_sel_hi:[1,0,1]
	v_mov_b32_e32 v160, v231
	v_pk_fma_f32 v[158:159], v[74:75], v[160:161], v[158:159] op_sel_hi:[1,0,1]
	ds_read_b128 v[224:227], v182 offset:36864
	s_waitcnt lgkmcnt(4)
	v_pk_fma_f32 v[164:165], v[124:125], v[232:233], 0 op_sel_hi:[1,0,0]
	s_nop 0
	v_pk_fma_f32 v[160:161], v[126:127], v[232:233], v[164:165] op_sel:[0,1,0]
	s_nop 0
	v_pk_fma_f32 v[160:161], v[128:129], v[234:235], v[160:161] op_sel_hi:[1,0,1]
	v_mov_b32_e32 v162, v235
	v_pk_fma_f32 v[164:165], v[130:131], v[162:163], v[160:161] op_sel_hi:[1,0,1]
	ds_read_b128 v[228:231], v182 offset:37888
	s_waitcnt lgkmcnt(4)
	v_pk_fma_f32 v[164:165], v[112:113], v[236:237], v[164:165] op_sel_hi:[1,0,1]
	s_nop 0
	v_pk_fma_f32 v[160:161], v[114:115], v[236:237], v[164:165] op_sel:[0,1,0]
	s_nop 0
	v_pk_fma_f32 v[160:161], v[118:119], v[238:239], v[160:161] op_sel_hi:[1,0,1]
	v_mov_b32_e32 v162, v239
	v_pk_fma_f32 v[164:165], v[122:123], v[162:163], v[160:161] op_sel_hi:[1,0,1]
	ds_read_b128 v[232:235], v182 offset:38912
	s_waitcnt lgkmcnt(4)
	v_pk_fma_f32 v[164:165], v[108:109], v[240:241], v[164:165] op_sel_hi:[1,0,1]
	s_nop 0
	v_pk_fma_f32 v[160:161], v[110:111], v[240:241], v[164:165] op_sel:[0,1,0]
	s_nop 0
	v_pk_fma_f32 v[160:161], v[116:117], v[242:243], v[160:161] op_sel_hi:[1,0,1]
	v_mov_b32_e32 v162, v243
	v_pk_fma_f32 v[164:165], v[120:121], v[162:163], v[160:161] op_sel_hi:[1,0,1]
	ds_read_b128 v[236:239], v182 offset:39936
	s_waitcnt lgkmcnt(4)
	v_pk_fma_f32 v[164:165], v[96:97], v[244:245], v[164:165] op_sel_hi:[1,0,1]
	s_nop 0
	v_pk_fma_f32 v[160:161], v[98:99], v[244:245], v[164:165] op_sel:[0,1,0]
	s_nop 0
	v_pk_fma_f32 v[160:161], v[102:103], v[246:247], v[160:161] op_sel_hi:[1,0,1]
	v_mov_b32_e32 v162, v247
	v_pk_fma_f32 v[164:165], v[106:107], v[162:163], v[160:161] op_sel_hi:[1,0,1]
	ds_read_b128 v[240:243], v182 offset:40960
	s_waitcnt lgkmcnt(4)
	v_pk_fma_f32 v[164:165], v[92:93], v[224:225], v[164:165] op_sel_hi:[1,0,1]
	s_nop 0
	v_pk_fma_f32 v[160:161], v[94:95], v[224:225], v[164:165] op_sel:[0,1,0]
	s_nop 0
	v_pk_fma_f32 v[160:161], v[100:101], v[226:227], v[160:161] op_sel_hi:[1,0,1]
	v_mov_b32_e32 v162, v227
	v_pk_fma_f32 v[164:165], v[104:105], v[162:163], v[160:161] op_sel_hi:[1,0,1]
	ds_read_b128 v[244:247], v182 offset:41984
	s_waitcnt lgkmcnt(4)
	v_pk_fma_f32 v[164:165], v[80:81], v[228:229], v[164:165] op_sel_hi:[1,0,1]
	s_nop 0
	v_pk_fma_f32 v[160:161], v[82:83], v[228:229], v[164:165] op_sel:[0,1,0]
	s_nop 0
	v_pk_fma_f32 v[160:161], v[86:87], v[230:231], v[160:161] op_sel_hi:[1,0,1]
	v_mov_b32_e32 v162, v231
	v_pk_fma_f32 v[164:165], v[90:91], v[162:163], v[160:161] op_sel_hi:[1,0,1]
	ds_read_b128 v[224:227], v182 offset:43008
	s_waitcnt lgkmcnt(4)
	v_pk_fma_f32 v[164:165], v[76:77], v[232:233], v[164:165] op_sel_hi:[1,0,1]
	s_nop 0
	v_pk_fma_f32 v[160:161], v[78:79], v[232:233], v[164:165] op_sel:[0,1,0]
	s_nop 0
	v_pk_fma_f32 v[160:161], v[84:85], v[234:235], v[160:161] op_sel_hi:[1,0,1]
	v_mov_b32_e32 v162, v235
	v_pk_fma_f32 v[164:165], v[88:89], v[162:163], v[160:161] op_sel_hi:[1,0,1]
	ds_read_b128 v[228:231], v182 offset:44032
	s_waitcnt lgkmcnt(4)
	v_pk_fma_f32 v[164:165], v[68:69], v[236:237], v[164:165] op_sel_hi:[1,0,1]
	s_nop 0
	v_pk_fma_f32 v[160:161], v[70:71], v[236:237], v[164:165] op_sel:[0,1,0]
	s_nop 0
	v_pk_fma_f32 v[160:161], v[72:73], v[238:239], v[160:161] op_sel_hi:[1,0,1]
	v_mov_b32_e32 v162, v239
	v_pk_fma_f32 v[160:161], v[74:75], v[162:163], v[160:161] op_sel_hi:[1,0,1]
	ds_read_b128 v[232:235], v182 offset:45056
	s_waitcnt lgkmcnt(4)
	v_pk_fma_f32 v[166:167], v[124:125], v[240:241], 0 op_sel_hi:[1,0,0]
	s_nop 0
	v_pk_fma_f32 v[162:163], v[126:127], v[240:241], v[166:167] op_sel:[0,1,0]
	s_nop 0
	v_pk_fma_f32 v[162:163], v[128:129], v[242:243], v[162:163] op_sel_hi:[1,0,1]
	v_mov_b32_e32 v164, v243
	v_pk_fma_f32 v[166:167], v[130:131], v[164:165], v[162:163] op_sel_hi:[1,0,1]
	ds_read_b128 v[236:239], v182 offset:46080
	s_waitcnt lgkmcnt(4)
; #define LAS __attribute__((address_space(3)))
; __device__ __forceinline__ void phase_norm2(const Params& p, const Ctx& F, const int l) {
;     ...
; #pragma unroll
;         for (int e = 0; e < 16; ++e) { f32x2 a = {0.f, 0.f};
; #pragma unroll
;             for (int j = 0; j < 8; ++j) { const f32x4 w = *((const LAS f32x4*)(wr2 + e * DM) + F.lane + 64 * j);
; #pragma unroll
;                 for (int c = 0; c < 4; ++c) a += vv[j][c] * w[c]; }
;             lg[e] = a; }
	v_pk_fma_f32 v[166:167], v[112:113], v[244:245], v[166:167] op_sel_hi:[1,0,1]
	s_nop 0
	v_pk_fma_f32 v[162:163], v[114:115], v[244:245], v[166:167] op_sel:[0,1,0]
	s_nop 0
	v_pk_fma_f32 v[162:163], v[118:119], v[246:247], v[162:163] op_sel_hi:[1,0,1]
	v_mov_b32_e32 v164, v247
	v_pk_fma_f32 v[166:167], v[122:123], v[164:165], v[162:163] op_sel_hi:[1,0,1]
	ds_read_b128 v[240:243], v182 offset:47104
	s_waitcnt lgkmcnt(4)
	v_pk_fma_f32 v[166:167], v[108:109], v[224:225], v[166:167] op_sel_hi:[1,0,1]
	s_nop 0
	v_pk_fma_f32 v[162:163], v[110:111], v[224:225], v[166:167] op_sel:[0,1,0]
	s_nop 0
	v_pk_fma_f32 v[162:163], v[116:117], v[226:227], v[162:163] op_sel_hi:[1,0,1]
	v_mov_b32_e32 v164, v227
	v_pk_fma_f32 v[166:167], v[120:121], v[164:165], v[162:163] op_sel_hi:[1,0,1]
	ds_read_b128 v[244:247], v182 offset:48128
	s_waitcnt lgkmcnt(4)
	v_pk_fma_f32 v[166:167], v[96:97], v[228:229], v[166:167] op_sel_hi:[1,0,1]
	s_nop 0
	v_pk_fma_f32 v[162:163], v[98:99], v[228:229], v[166:167] op_sel:[0,1,0]
	s_nop 0
	v_pk_fma_f32 v[162:163], v[102:103], v[230:231], v[162:163] op_sel_hi:[1,0,1]
	v_mov_b32_e32 v164, v231
	v_pk_fma_f32 v[166:167], v[106:107], v[164:165], v[162:163] op_sel_hi:[1,0,1]
	ds_read_b128 v[224:227], v182 offset:49152
	s_waitcnt lgkmcnt(4)
	v_pk_fma_f32 v[166:167], v[92:93], v[232:233], v[166:167] op_sel_hi:[1,0,1]
	s_nop 0
	v_pk_fma_f32 v[162:163], v[94:95], v[232:233], v[166:167] op_sel:[0,1,0]
	s_nop 0
	v_pk_fma_f32 v[162:163], v[100:101], v[234:235], v[162:163] op_sel_hi:[1,0,1]
	v_mov_b32_e32 v164, v235
	v_pk_fma_f32 v[166:167], v[104:105], v[164:165], v[162:163] op_sel_hi:[1,0,1]
	ds_read_b128 v[228:231], v182 offset:50176
	s_waitcnt lgkmcnt(4)
	v_pk_fma_f32 v[166:167], v[80:81], v[236:237], v[166:167] op_sel_hi:[1,0,1]
	s_nop 0
	v_pk_fma_f32 v[162:163], v[82:83], v[236:237], v[166:167] op_sel:[0,1,0]
	s_nop 0
	v_pk_fma_f32 v[162:163], v[86:87], v[238:239], v[162:163] op_sel_hi:[1,0,1]
	v_mov_b32_e32 v164, v239
	v_pk_fma_f32 v[166:167], v[90:91], v[164:165], v[162:163] op_sel_hi:[1,0,1]
	ds_read_b128 v[232:235], v182 offset:51200
	s_waitcnt lgkmcnt(4)
	v_pk_fma_f32 v[166:167], v[76:77], v[240:241], v[166:167] op_sel_hi:[1,0,1]
	s_nop 0
	v_pk_fma_f32 v[162:163], v[78:79], v[240:241], v[166:167] op_sel:[0,1,0]
	s_nop 0
	v_pk_fma_f32 v[162:163], v[84:85], v[242:243], v[162:163] op_sel_hi:[1,0,1]
	v_mov_b32_e32 v164, v243
	v_pk_fma_f32 v[166:167], v[88:89], v[164:165], v[162:163] op_sel_hi:[1,0,1]
	ds_read_b128 v[236:239], v182 offset:52224
	s_waitcnt lgkmcnt(4)
	v_pk_fma_f32 v[166:167], v[68:69], v[244:245], v[166:167] op_sel_hi:[1,0,1]
	s_nop 0
	v_pk_fma_f32 v[162:163], v[70:71], v[244:245], v[166:167] op_sel:[0,1,0]
	s_nop 0
	v_pk_fma_f32 v[162:163], v[72:73], v[246:247], v[162:163] op_sel_hi:[1,0,1]
	v_mov_b32_e32 v164, v247
	v_pk_fma_f32 v[162:163], v[74:75], v[164:165], v[162:163] op_sel_hi:[1,0,1]
	ds_read_b128 v[240:243], v182 offset:53248
	s_waitcnt lgkmcnt(4)
	v_pk_fma_f32 v[168:169], v[124:125], v[224:225], 0 op_sel_hi:[1,0,0]
	s_nop 0
	v_pk_fma_f32 v[164:165], v[126:127], v[224:225], v[168:169] op_sel:[0,1,0]
	s_nop 0
	v_pk_fma_f32 v[164:165], v[128:129], v[226:227], v[164:165] op_sel_hi:[1,0,1]
	v_mov_b32_e32 v166, v227
	v_pk_fma_f32 v[168:169], v[130:131], v[166:167], v[164:165] op_sel_hi:[1,0,1]
	ds_read_b128 v[244:247], v182 offset:54272
	s_waitcnt lgkmcnt(4)
	v_pk_fma_f32 v[168:169], v[112:113], v[228:229], v[168:169] op_sel_hi:[1,0,1]
	s_nop 0
	v_pk_fma_f32 v[164:165], v[114:115], v[228:229], v[168:169] op_sel:[0,1,0]
	s_nop 0
	v_pk_fma_f32 v[164:165], v[118:119], v[230:231], v[164:165] op_sel_hi:[1,0,1]
	v_mov_b32_e32 v166, v231
	v_pk_fma_f32 v[168:169], v[122:123], v[166:167], v[164:165] op_sel_hi:[1,0,1]
	ds_read_b128 v[224:227], v182 offset:55296
	s_waitcnt lgkmcnt(4)
	v_pk_fma_f32 v[168:169], v[108:109], v[232:233], v[168:169] op_sel_hi:[1,0,1]
	s_nop 0
	v_pk_fma_f32 v[164:165], v[110:111], v[232:233], v[168:169] op_sel:[0,1,0]
	s_nop 0
	v_pk_fma_f32 v[164:165], v[116:117], v[234:235], v[164:165] op_sel_hi:[1,0,1]
	v_mov_b32_e32 v166, v235
	v_pk_fma_f32 v[168:169], v[120:121], v[166:167], v[164:165] op_sel_hi:[1,0,1]
	ds_read_b128 v[228:231], v182 offset:56320
	s_waitcnt lgkmcnt(4)
	v_pk_fma_f32 v[168:169], v[96:97], v[236:237], v[168:169] op_sel_hi:[1,0,1]
	s_nop 0
	v_pk_fma_f32 v[164:165], v[98:99], v[236:237], v[168:169] op_sel:[0,1,0]
	s_nop 0
	v_pk_fma_f32 v[164:165], v[102:103], v[238:239], v[164:165] op_sel_hi:[1,0,1]
	v_mov_b32_e32 v166, v239
	v_pk_fma_f32 v[168:169], v[106:107], v[166:167], v[164:165] op_sel_hi:[1,0,1]
	ds_read_b128 v[232:235], v182 offset:57344
	s_waitcnt lgkmcnt(4)
	v_pk_fma_f32 v[168:169], v[92:93], v[240:241], v[168:169] op_sel_hi:[1,0,1]
	s_nop 0
	v_pk_fma_f32 v[164:165], v[94:95], v[240:241], v[168:169] op_sel:[0,1,0]
	s_nop 0
	v_pk_fma_f32 v[164:165], v[100:101], v[242:243], v[164:165] op_sel_hi:[1,0,1]
	v_mov_b32_e32 v166, v243
	v_pk_fma_f32 v[168:169], v[104:105], v[166:167], v[164:165] op_sel_hi:[1,0,1]
	ds_read_b128 v[236:239], v182 offset:58368
	s_waitcnt lgkmcnt(4)
	v_pk_fma_f32 v[168:169], v[80:81], v[244:245], v[168:169] op_sel_hi:[1,0,1]
	s_nop 0
	v_pk_fma_f32 v[164:165], v[82:83], v[244:245], v[168:169] op_sel:[0,1,0]
	s_nop 0
	v_pk_fma_f32 v[164:165], v[86:87], v[246:247], v[164:165] op_sel_hi:[1,0,1]
	v_mov_b32_e32 v166, v247
	v_pk_fma_f32 v[168:169], v[90:91], v[166:167], v[164:165] op_sel_hi:[1,0,1]
	ds_read_b128 v[240:243], v182 offset:59392
	s_waitcnt lgkmcnt(4)
; #define LAS __attribute__((address_space(3)))
; __device__ __forceinline__ void phase_norm2(const Params& p, const Ctx& F, const int l) {
;     ...
; #pragma unroll
;         for (int e = 0; e < 16; ++e) { f32x2 a = {0.f, 0.f};
; #pragma unroll
;             for (int j = 0; j < 8; ++j) { const f32x4 w = *((const LAS f32x4*)(wr2 + e * DM) + F.lane + 64 * j);
; #pragma unroll
;                 for (int c = 0; c < 4; ++c) a += vv[j][c] * w[c]; }
;             lg[e] = a; }
	v_pk_fma_f32 v[168:169], v[76:77], v[224:225], v[168:169] op_sel_hi:[1,0,1]
	s_nop 0
	v_pk_fma_f32 v[164:165], v[78:79], v[224:225], v[168:169] op_sel:[0,1,0]
	s_nop 0
	v_pk_fma_f32 v[164:165], v[84:85], v[226:227], v[164:165] op_sel_hi:[1,0,1]
	v_mov_b32_e32 v166, v227
	v_pk_fma_f32 v[168:169], v[88:89], v[166:167], v[164:165] op_sel_hi:[1,0,1]
	ds_read_b128 v[244:247], v182 offset:60416
	s_waitcnt lgkmcnt(4)
	v_pk_fma_f32 v[168:169], v[68:69], v[228:229], v[168:169] op_sel_hi:[1,0,1]
	s_nop 0
	v_pk_fma_f32 v[164:165], v[70:71], v[228:229], v[168:169] op_sel:[0,1,0]
	s_nop 0
	v_pk_fma_f32 v[164:165], v[72:73], v[230:231], v[164:165] op_sel_hi:[1,0,1]
	v_mov_b32_e32 v166, v231
	v_pk_fma_f32 v[164:165], v[74:75], v[166:167], v[164:165] op_sel_hi:[1,0,1]
	ds_read_b128 v[224:227], v182 offset:61440
	s_waitcnt lgkmcnt(4)
	v_pk_fma_f32 v[170:171], v[124:125], v[232:233], 0 op_sel_hi:[1,0,0]
	s_nop 0
	v_pk_fma_f32 v[166:167], v[126:127], v[232:233], v[170:171] op_sel:[0,1,0]
	s_nop 0
	v_pk_fma_f32 v[166:167], v[128:129], v[234:235], v[166:167] op_sel_hi:[1,0,1]
	v_mov_b32_e32 v168, v235
	v_pk_fma_f32 v[170:171], v[130:131], v[168:169], v[166:167] op_sel_hi:[1,0,1]
	ds_read_b128 v[228:231], v182 offset:62464
	s_waitcnt lgkmcnt(4)
	v_pk_fma_f32 v[170:171], v[112:113], v[236:237], v[170:171] op_sel_hi:[1,0,1]
	s_nop 0
	v_pk_fma_f32 v[166:167], v[114:115], v[236:237], v[170:171] op_sel:[0,1,0]
	s_nop 0
	v_pk_fma_f32 v[166:167], v[118:119], v[238:239], v[166:167] op_sel_hi:[1,0,1]
	v_mov_b32_e32 v168, v239
	v_pk_fma_f32 v[170:171], v[122:123], v[168:169], v[166:167] op_sel_hi:[1,0,1]
	ds_read_b128 v[232:235], v182 offset:63488
	s_waitcnt lgkmcnt(4)
	v_pk_fma_f32 v[170:171], v[108:109], v[240:241], v[170:171] op_sel_hi:[1,0,1]
	s_nop 0
	v_pk_fma_f32 v[166:167], v[110:111], v[240:241], v[170:171] op_sel:[0,1,0]
	s_nop 0
	v_pk_fma_f32 v[166:167], v[116:117], v[242:243], v[166:167] op_sel_hi:[1,0,1]
	v_mov_b32_e32 v168, v243
	v_pk_fma_f32 v[170:171], v[120:121], v[168:169], v[166:167] op_sel_hi:[1,0,1]
	ds_read_b128 v[236:239], v182 offset:64512
	s_waitcnt lgkmcnt(4)
	v_pk_fma_f32 v[170:171], v[96:97], v[244:245], v[170:171] op_sel_hi:[1,0,1]
	s_nop 0
	v_pk_fma_f32 v[166:167], v[98:99], v[244:245], v[170:171] op_sel:[0,1,0]
	s_nop 0
	v_pk_fma_f32 v[166:167], v[102:103], v[246:247], v[166:167] op_sel_hi:[1,0,1]
	v_mov_b32_e32 v168, v247
	v_pk_fma_f32 v[170:171], v[106:107], v[168:169], v[166:167] op_sel_hi:[1,0,1]
	ds_read_b128 v[240:243], v202
	s_waitcnt lgkmcnt(4)
	v_pk_fma_f32 v[170:171], v[92:93], v[224:225], v[170:171] op_sel_hi:[1,0,1]
	s_nop 0
	v_pk_fma_f32 v[166:167], v[94:95], v[224:225], v[170:171] op_sel:[0,1,0]
	s_nop 0
	v_pk_fma_f32 v[166:167], v[100:101], v[226:227], v[166:167] op_sel_hi:[1,0,1]
	v_mov_b32_e32 v168, v227
	v_pk_fma_f32 v[170:171], v[104:105], v[168:169], v[166:167] op_sel_hi:[1,0,1]
	ds_read_b128 v[244:247], v202 offset:1024
	s_waitcnt lgkmcnt(4)
	v_pk_fma_f32 v[170:171], v[80:81], v[228:229], v[170:171] op_sel_hi:[1,0,1]
	s_nop 0
	v_pk_fma_f32 v[166:167], v[82:83], v[228:229], v[170:171] op_sel:[0,1,0]
	s_nop 0
	v_pk_fma_f32 v[166:167], v[86:87], v[230:231], v[166:167] op_sel_hi:[1,0,1]
	v_mov_b32_e32 v168, v231
	v_pk_fma_f32 v[170:171], v[90:91], v[168:169], v[166:167] op_sel_hi:[1,0,1]
	ds_read_b128 v[224:227], v202 offset:2048
	s_waitcnt lgkmcnt(4)
	v_pk_fma_f32 v[170:171], v[76:77], v[232:233], v[170:171] op_sel_hi:[1,0,1]
	s_nop 0
	v_pk_fma_f32 v[166:167], v[78:79], v[232:233], v[170:171] op_sel:[0,1,0]
	s_nop 0
	v_pk_fma_f32 v[166:167], v[84:85], v[234:235], v[166:167] op_sel_hi:[1,0,1]
	v_mov_b32_e32 v168, v235
	v_pk_fma_f32 v[170:171], v[88:89], v[168:169], v[166:167] op_sel_hi:[1,0,1]
	ds_read_b128 v[228:231], v202 offset:3072
	s_waitcnt lgkmcnt(4)
	v_pk_fma_f32 v[170:171], v[68:69], v[236:237], v[170:171] op_sel_hi:[1,0,1]
	s_nop 0
	v_pk_fma_f32 v[166:167], v[70:71], v[236:237], v[170:171] op_sel:[0,1,0]
	s_nop 0
	v_pk_fma_f32 v[166:167], v[72:73], v[238:239], v[166:167] op_sel_hi:[1,0,1]
	v_mov_b32_e32 v168, v239
	v_pk_fma_f32 v[166:167], v[74:75], v[168:169], v[166:167] op_sel_hi:[1,0,1]
	ds_read_b128 v[232:235], v202 offset:4096
	s_waitcnt lgkmcnt(4)
	v_pk_fma_f32 v[172:173], v[124:125], v[240:241], 0 op_sel_hi:[1,0,0]
	s_nop 0
	v_pk_fma_f32 v[168:169], v[126:127], v[240:241], v[172:173] op_sel:[0,1,0]
	s_nop 0
	v_pk_fma_f32 v[168:169], v[128:129], v[242:243], v[168:169] op_sel_hi:[1,0,1]
	v_mov_b32_e32 v170, v243
	v_pk_fma_f32 v[172:173], v[130:131], v[170:171], v[168:169] op_sel_hi:[1,0,1]
	ds_read_b128 v[236:239], v202 offset:5120
	s_waitcnt lgkmcnt(4)
	v_pk_fma_f32 v[172:173], v[112:113], v[244:245], v[172:173] op_sel_hi:[1,0,1]
	s_nop 0
	v_pk_fma_f32 v[168:169], v[114:115], v[244:245], v[172:173] op_sel:[0,1,0]
	s_nop 0
	v_pk_fma_f32 v[168:169], v[118:119], v[246:247], v[168:169] op_sel_hi:[1,0,1]
	v_mov_b32_e32 v170, v247
	v_pk_fma_f32 v[172:173], v[122:123], v[170:171], v[168:169] op_sel_hi:[1,0,1]
	ds_read_b128 v[240:243], v202 offset:6144
	s_waitcnt lgkmcnt(4)
	v_pk_fma_f32 v[172:173], v[108:109], v[224:225], v[172:173] op_sel_hi:[1,0,1]
	s_nop 0
	v_pk_fma_f32 v[168:169], v[110:111], v[224:225], v[172:173] op_sel:[0,1,0]
	s_nop 0
	v_pk_fma_f32 v[168:169], v[116:117], v[226:227], v[168:169] op_sel_hi:[1,0,1]
	v_mov_b32_e32 v170, v227
	v_pk_fma_f32 v[172:173], v[120:121], v[170:171], v[168:169] op_sel_hi:[1,0,1]
	ds_read_b128 v[244:247], v202 offset:7168
	s_waitcnt lgkmcnt(4)
	v_pk_fma_f32 v[172:173], v[96:97], v[228:229], v[172:173] op_sel_hi:[1,0,1]
	s_nop 0
	v_pk_fma_f32 v[168:169], v[98:99], v[228:229], v[172:173] op_sel:[0,1,0]
	s_nop 0
	v_pk_fma_f32 v[168:169], v[102:103], v[230:231], v[168:169] op_sel_hi:[1,0,1]
	v_mov_b32_e32 v170, v231
	v_pk_fma_f32 v[172:173], v[106:107], v[170:171], v[168:169] op_sel_hi:[1,0,1]
	ds_read_b128 v[224:227], v202 offset:8192
	s_waitcnt lgkmcnt(4)
; #define LAS __attribute__((address_space(3)))
; __device__ __forceinline__ void phase_norm2(const Params& p, const Ctx& F, const int l) {
;     ...
; #pragma unroll
;         for (int e = 0; e < 16; ++e) { f32x2 a = {0.f, 0.f};
; #pragma unroll
;             for (int j = 0; j < 8; ++j) { const f32x4 w = *((const LAS f32x4*)(wr2 + e * DM) + F.lane + 64 * j);
; #pragma unroll
;                 for (int c = 0; c < 4; ++c) a += vv[j][c] * w[c]; }
;             lg[e] = a; }
	v_pk_fma_f32 v[172:173], v[92:93], v[232:233], v[172:173] op_sel_hi:[1,0,1]
	s_nop 0
	v_pk_fma_f32 v[168:169], v[94:95], v[232:233], v[172:173] op_sel:[0,1,0]
	s_nop 0
	v_pk_fma_f32 v[168:169], v[100:101], v[234:235], v[168:169] op_sel_hi:[1,0,1]
	v_mov_b32_e32 v170, v235
	v_pk_fma_f32 v[172:173], v[104:105], v[170:171], v[168:169] op_sel_hi:[1,0,1]
	ds_read_b128 v[228:231], v202 offset:9216
	s_waitcnt lgkmcnt(4)
	v_pk_fma_f32 v[172:173], v[80:81], v[236:237], v[172:173] op_sel_hi:[1,0,1]
	s_nop 0
	v_pk_fma_f32 v[168:169], v[82:83], v[236:237], v[172:173] op_sel:[0,1,0]
	s_nop 0
	v_pk_fma_f32 v[168:169], v[86:87], v[238:239], v[168:169] op_sel_hi:[1,0,1]
	v_mov_b32_e32 v170, v239
	v_pk_fma_f32 v[172:173], v[90:91], v[170:171], v[168:169] op_sel_hi:[1,0,1]
	ds_read_b128 v[232:235], v202 offset:10240
	s_waitcnt lgkmcnt(4)
	v_pk_fma_f32 v[172:173], v[76:77], v[240:241], v[172:173] op_sel_hi:[1,0,1]
	s_nop 0
	v_pk_fma_f32 v[168:169], v[78:79], v[240:241], v[172:173] op_sel:[0,1,0]
	s_nop 0
	v_pk_fma_f32 v[168:169], v[84:85], v[242:243], v[168:169] op_sel_hi:[1,0,1]
	v_mov_b32_e32 v170, v243
	v_pk_fma_f32 v[172:173], v[88:89], v[170:171], v[168:169] op_sel_hi:[1,0,1]
	ds_read_b128 v[236:239], v202 offset:11264
	s_waitcnt lgkmcnt(4)
	v_pk_fma_f32 v[172:173], v[68:69], v[244:245], v[172:173] op_sel_hi:[1,0,1]
	s_nop 0
	v_pk_fma_f32 v[168:169], v[70:71], v[244:245], v[172:173] op_sel:[0,1,0]
	s_nop 0
	v_pk_fma_f32 v[168:169], v[72:73], v[246:247], v[168:169] op_sel_hi:[1,0,1]
	v_mov_b32_e32 v170, v247
	v_pk_fma_f32 v[168:169], v[74:75], v[170:171], v[168:169] op_sel_hi:[1,0,1]
	ds_read_b128 v[240:243], v202 offset:12288
	s_waitcnt lgkmcnt(4)
	v_pk_fma_f32 v[174:175], v[124:125], v[224:225], 0 op_sel_hi:[1,0,0]
	s_nop 0
	v_pk_fma_f32 v[170:171], v[126:127], v[224:225], v[174:175] op_sel:[0,1,0]
	s_nop 0
	v_pk_fma_f32 v[170:171], v[128:129], v[226:227], v[170:171] op_sel_hi:[1,0,1]
	v_mov_b32_e32 v172, v227
	v_pk_fma_f32 v[174:175], v[130:131], v[172:173], v[170:171] op_sel_hi:[1,0,1]
	ds_read_b128 v[244:247], v202 offset:13312
	s_waitcnt lgkmcnt(4)
	v_pk_fma_f32 v[174:175], v[112:113], v[228:229], v[174:175] op_sel_hi:[1,0,1]
	s_nop 0
	v_pk_fma_f32 v[170:171], v[114:115], v[228:229], v[174:175] op_sel:[0,1,0]
	s_nop 0
	v_pk_fma_f32 v[170:171], v[118:119], v[230:231], v[170:171] op_sel_hi:[1,0,1]
	v_mov_b32_e32 v172, v231
	v_pk_fma_f32 v[174:175], v[122:123], v[172:173], v[170:171] op_sel_hi:[1,0,1]
	ds_read_b128 v[224:227], v202 offset:14336
	s_waitcnt lgkmcnt(4)
	v_pk_fma_f32 v[174:175], v[108:109], v[232:233], v[174:175] op_sel_hi:[1,0,1]
	s_nop 0
	v_pk_fma_f32 v[170:171], v[110:111], v[232:233], v[174:175] op_sel:[0,1,0]
	s_nop 0
	v_pk_fma_f32 v[170:171], v[116:117], v[234:235], v[170:171] op_sel_hi:[1,0,1]
	v_mov_b32_e32 v172, v235
	v_pk_fma_f32 v[174:175], v[120:121], v[172:173], v[170:171] op_sel_hi:[1,0,1]
	ds_read_b128 v[228:231], v202 offset:15360
	s_waitcnt lgkmcnt(4)
	v_pk_fma_f32 v[174:175], v[96:97], v[236:237], v[174:175] op_sel_hi:[1,0,1]
	s_nop 0
	v_pk_fma_f32 v[170:171], v[98:99], v[236:237], v[174:175] op_sel:[0,1,0]
	s_nop 0
	v_pk_fma_f32 v[170:171], v[102:103], v[238:239], v[170:171] op_sel_hi:[1,0,1]
	v_mov_b32_e32 v172, v239
	v_pk_fma_f32 v[174:175], v[106:107], v[172:173], v[170:171] op_sel_hi:[1,0,1]
	ds_read_b128 v[232:235], v202 offset:16384
	s_waitcnt lgkmcnt(4)
	v_pk_fma_f32 v[174:175], v[92:93], v[240:241], v[174:175] op_sel_hi:[1,0,1]
	s_nop 0
	v_pk_fma_f32 v[170:171], v[94:95], v[240:241], v[174:175] op_sel:[0,1,0]
	s_nop 0
	v_pk_fma_f32 v[170:171], v[100:101], v[242:243], v[170:171] op_sel_hi:[1,0,1]
	v_mov_b32_e32 v172, v243
	v_pk_fma_f32 v[174:175], v[104:105], v[172:173], v[170:171] op_sel_hi:[1,0,1]
	ds_read_b128 v[236:239], v202 offset:17408
	s_waitcnt lgkmcnt(4)
	v_pk_fma_f32 v[174:175], v[80:81], v[244:245], v[174:175] op_sel_hi:[1,0,1]
	s_nop 0
	v_pk_fma_f32 v[170:171], v[82:83], v[244:245], v[174:175] op_sel:[0,1,0]
	s_nop 0
	v_pk_fma_f32 v[170:171], v[86:87], v[246:247], v[170:171] op_sel_hi:[1,0,1]
	v_mov_b32_e32 v172, v247
	v_pk_fma_f32 v[174:175], v[90:91], v[172:173], v[170:171] op_sel_hi:[1,0,1]
	ds_read_b128 v[240:243], v202 offset:18432
	s_waitcnt lgkmcnt(4)
	v_pk_fma_f32 v[174:175], v[76:77], v[224:225], v[174:175] op_sel_hi:[1,0,1]
	s_nop 0
	v_pk_fma_f32 v[170:171], v[78:79], v[224:225], v[174:175] op_sel:[0,1,0]
	s_nop 0
	v_pk_fma_f32 v[170:171], v[84:85], v[226:227], v[170:171] op_sel_hi:[1,0,1]
	v_mov_b32_e32 v172, v227
	v_pk_fma_f32 v[174:175], v[88:89], v[172:173], v[170:171] op_sel_hi:[1,0,1]
	ds_read_b128 v[244:247], v202 offset:19456
	s_waitcnt lgkmcnt(4)
	v_pk_fma_f32 v[174:175], v[68:69], v[228:229], v[174:175] op_sel_hi:[1,0,1]
	s_nop 0
	v_pk_fma_f32 v[170:171], v[70:71], v[228:229], v[174:175] op_sel:[0,1,0]
	s_nop 0
	v_pk_fma_f32 v[170:171], v[72:73], v[230:231], v[170:171] op_sel_hi:[1,0,1]
	v_mov_b32_e32 v172, v231
	v_pk_fma_f32 v[170:171], v[74:75], v[172:173], v[170:171] op_sel_hi:[1,0,1]
	ds_read_b128 v[224:227], v202 offset:20480
	s_waitcnt lgkmcnt(4)
	v_pk_fma_f32 v[176:177], v[124:125], v[232:233], 0 op_sel_hi:[1,0,0]
	s_nop 0
	v_pk_fma_f32 v[172:173], v[126:127], v[232:233], v[176:177] op_sel:[0,1,0]
	s_nop 0
	v_pk_fma_f32 v[172:173], v[128:129], v[234:235], v[172:173] op_sel_hi:[1,0,1]
	v_mov_b32_e32 v174, v235
	v_pk_fma_f32 v[176:177], v[130:131], v[174:175], v[172:173] op_sel_hi:[1,0,1]
	ds_read_b128 v[228:231], v202 offset:21504
	s_waitcnt lgkmcnt(4)
	v_pk_fma_f32 v[176:177], v[112:113], v[236:237], v[176:177] op_sel_hi:[1,0,1]
	s_nop 0
	v_pk_fma_f32 v[172:173], v[114:115], v[236:237], v[176:177] op_sel:[0,1,0]
	s_nop 0
	v_pk_fma_f32 v[172:173], v[118:119], v[238:239], v[172:173] op_sel_hi:[1,0,1]
	v_mov_b32_e32 v174, v239
	v_pk_fma_f32 v[176:177], v[122:123], v[174:175], v[172:173] op_sel_hi:[1,0,1]
	ds_read_b128 v[232:235], v202 offset:22528
	s_waitcnt lgkmcnt(4)
; #define LAS __attribute__((address_space(3)))
; __device__ __forceinline__ void phase_norm2(const Params& p, const Ctx& F, const int l) {
;     ...
; #pragma unroll
;         for (int e = 0; e < 16; ++e) { f32x2 a = {0.f, 0.f};
; #pragma unroll
;             for (int j = 0; j < 8; ++j) { const f32x4 w = *((const LAS f32x4*)(wr2 + e * DM) + F.lane + 64 * j);
; #pragma unroll
;                 for (int c = 0; c < 4; ++c) a += vv[j][c] * w[c]; }
;             lg[e] = a; }
	v_pk_fma_f32 v[176:177], v[108:109], v[240:241], v[176:177] op_sel_hi:[1,0,1]
	s_nop 0
	v_pk_fma_f32 v[172:173], v[110:111], v[240:241], v[176:177] op_sel:[0,1,0]
	s_nop 0
	v_pk_fma_f32 v[172:173], v[116:117], v[242:243], v[172:173] op_sel_hi:[1,0,1]
	v_mov_b32_e32 v174, v243
	v_pk_fma_f32 v[176:177], v[120:121], v[174:175], v[172:173] op_sel_hi:[1,0,1]
	ds_read_b128 v[236:239], v202 offset:23552
	s_waitcnt lgkmcnt(4)
	v_pk_fma_f32 v[176:177], v[96:97], v[244:245], v[176:177] op_sel_hi:[1,0,1]
	s_nop 0
	v_pk_fma_f32 v[172:173], v[98:99], v[244:245], v[176:177] op_sel:[0,1,0]
	s_nop 0
	v_pk_fma_f32 v[172:173], v[102:103], v[246:247], v[172:173] op_sel_hi:[1,0,1]
	v_mov_b32_e32 v174, v247
	v_pk_fma_f32 v[176:177], v[106:107], v[174:175], v[172:173] op_sel_hi:[1,0,1]
	ds_read_b128 v[240:243], v202 offset:24576
	s_waitcnt lgkmcnt(4)
	v_pk_fma_f32 v[176:177], v[92:93], v[224:225], v[176:177] op_sel_hi:[1,0,1]
	s_nop 0
	v_pk_fma_f32 v[172:173], v[94:95], v[224:225], v[176:177] op_sel:[0,1,0]
	s_nop 0
	v_pk_fma_f32 v[172:173], v[100:101], v[226:227], v[172:173] op_sel_hi:[1,0,1]
	v_mov_b32_e32 v174, v227
	v_pk_fma_f32 v[176:177], v[104:105], v[174:175], v[172:173] op_sel_hi:[1,0,1]
	ds_read_b128 v[244:247], v202 offset:25600
	s_waitcnt lgkmcnt(4)
	v_pk_fma_f32 v[176:177], v[80:81], v[228:229], v[176:177] op_sel_hi:[1,0,1]
	s_nop 0
	v_pk_fma_f32 v[172:173], v[82:83], v[228:229], v[176:177] op_sel:[0,1,0]
	s_nop 0
	v_pk_fma_f32 v[172:173], v[86:87], v[230:231], v[172:173] op_sel_hi:[1,0,1]
	v_mov_b32_e32 v174, v231
	v_pk_fma_f32 v[176:177], v[90:91], v[174:175], v[172:173] op_sel_hi:[1,0,1]
	ds_read_b128 v[224:227], v202 offset:26624
	s_waitcnt lgkmcnt(4)
	v_pk_fma_f32 v[176:177], v[76:77], v[232:233], v[176:177] op_sel_hi:[1,0,1]
	s_nop 0
	v_pk_fma_f32 v[172:173], v[78:79], v[232:233], v[176:177] op_sel:[0,1,0]
	s_nop 0
	v_pk_fma_f32 v[172:173], v[84:85], v[234:235], v[172:173] op_sel_hi:[1,0,1]
	v_mov_b32_e32 v174, v235
	v_pk_fma_f32 v[176:177], v[88:89], v[174:175], v[172:173] op_sel_hi:[1,0,1]
	ds_read_b128 v[228:231], v202 offset:27648
	s_waitcnt lgkmcnt(4)
	v_pk_fma_f32 v[176:177], v[68:69], v[236:237], v[176:177] op_sel_hi:[1,0,1]
	s_nop 0
	v_pk_fma_f32 v[172:173], v[70:71], v[236:237], v[176:177] op_sel:[0,1,0]
	s_nop 0
	v_pk_fma_f32 v[172:173], v[72:73], v[238:239], v[172:173] op_sel_hi:[1,0,1]
	v_mov_b32_e32 v174, v239
	v_pk_fma_f32 v[172:173], v[74:75], v[174:175], v[172:173] op_sel_hi:[1,0,1]
	ds_read_b128 v[232:235], v202 offset:28672
	s_waitcnt lgkmcnt(4)
	v_pk_fma_f32 v[178:179], v[124:125], v[240:241], 0 op_sel_hi:[1,0,0]
	s_nop 0
	v_pk_fma_f32 v[174:175], v[126:127], v[240:241], v[178:179] op_sel:[0,1,0]
	s_nop 0
	v_pk_fma_f32 v[174:175], v[128:129], v[242:243], v[174:175] op_sel_hi:[1,0,1]
	v_mov_b32_e32 v176, v243
	v_pk_fma_f32 v[178:179], v[130:131], v[176:177], v[174:175] op_sel_hi:[1,0,1]
	ds_read_b128 v[236:239], v202 offset:29696
	s_waitcnt lgkmcnt(4)
	v_pk_fma_f32 v[178:179], v[112:113], v[244:245], v[178:179] op_sel_hi:[1,0,1]
	s_nop 0
	v_pk_fma_f32 v[174:175], v[114:115], v[244:245], v[178:179] op_sel:[0,1,0]
	s_nop 0
	v_pk_fma_f32 v[174:175], v[118:119], v[246:247], v[174:175] op_sel_hi:[1,0,1]
	v_mov_b32_e32 v176, v247
	v_pk_fma_f32 v[178:179], v[122:123], v[176:177], v[174:175] op_sel_hi:[1,0,1]
	ds_read_b128 v[240:243], v202 offset:30720
	s_waitcnt lgkmcnt(4)
	v_pk_fma_f32 v[178:179], v[108:109], v[224:225], v[178:179] op_sel_hi:[1,0,1]
	s_nop 0
	v_pk_fma_f32 v[174:175], v[110:111], v[224:225], v[178:179] op_sel:[0,1,0]
	s_nop 0
	v_pk_fma_f32 v[174:175], v[116:117], v[226:227], v[174:175] op_sel_hi:[1,0,1]
	v_mov_b32_e32 v176, v227
	v_pk_fma_f32 v[178:179], v[120:121], v[176:177], v[174:175] op_sel_hi:[1,0,1]
	ds_read_b128 v[244:247], v202 offset:31744
	s_waitcnt lgkmcnt(4)
	v_pk_fma_f32 v[178:179], v[96:97], v[228:229], v[178:179] op_sel_hi:[1,0,1]
	s_nop 0
	v_pk_fma_f32 v[174:175], v[98:99], v[228:229], v[178:179] op_sel:[0,1,0]
	s_nop 0
	v_pk_fma_f32 v[174:175], v[102:103], v[230:231], v[174:175] op_sel_hi:[1,0,1]
	v_mov_b32_e32 v176, v231
	v_pk_fma_f32 v[178:179], v[106:107], v[176:177], v[174:175] op_sel_hi:[1,0,1]
	ds_read_b128 v[224:227], v202 offset:32768
	s_waitcnt lgkmcnt(4)
	v_pk_fma_f32 v[178:179], v[92:93], v[232:233], v[178:179] op_sel_hi:[1,0,1]
	s_nop 0
	v_pk_fma_f32 v[174:175], v[94:95], v[232:233], v[178:179] op_sel:[0,1,0]
	s_nop 0
	v_pk_fma_f32 v[174:175], v[100:101], v[234:235], v[174:175] op_sel_hi:[1,0,1]
	v_mov_b32_e32 v176, v235
	v_pk_fma_f32 v[178:179], v[104:105], v[176:177], v[174:175] op_sel_hi:[1,0,1]
	ds_read_b128 v[228:231], v202 offset:33792
	s_waitcnt lgkmcnt(4)
	v_pk_fma_f32 v[178:179], v[80:81], v[236:237], v[178:179] op_sel_hi:[1,0,1]
	s_nop 0
	v_pk_fma_f32 v[174:175], v[82:83], v[236:237], v[178:179] op_sel:[0,1,0]
	s_nop 0
	v_pk_fma_f32 v[174:175], v[86:87], v[238:239], v[174:175] op_sel_hi:[1,0,1]
	v_mov_b32_e32 v176, v239
	v_pk_fma_f32 v[178:179], v[90:91], v[176:177], v[174:175] op_sel_hi:[1,0,1]
	ds_read_b128 v[232:235], v202 offset:34816
	s_waitcnt lgkmcnt(4)
	v_pk_fma_f32 v[178:179], v[76:77], v[240:241], v[178:179] op_sel_hi:[1,0,1]
	s_nop 0
	v_pk_fma_f32 v[174:175], v[78:79], v[240:241], v[178:179] op_sel:[0,1,0]
	s_nop 0
	v_pk_fma_f32 v[174:175], v[84:85], v[242:243], v[174:175] op_sel_hi:[1,0,1]
	v_mov_b32_e32 v176, v243
	v_pk_fma_f32 v[178:179], v[88:89], v[176:177], v[174:175] op_sel_hi:[1,0,1]
	ds_read_b128 v[236:239], v202 offset:35840
	s_waitcnt lgkmcnt(4)
; #define LAS __attribute__((address_space(3)))
; __device__ __forceinline__ void phase_norm2(const Params& p, const Ctx& F, const int l) {
;     ...
; #pragma unroll
;         for (int e = 0; e < 16; ++e) { f32x2 a = {0.f, 0.f};
; #pragma unroll
;             for (int j = 0; j < 8; ++j) { const f32x4 w = *((const LAS f32x4*)(wr2 + e * DM) + F.lane + 64 * j);
; #pragma unroll
;                 for (int c = 0; c < 4; ++c) a += vv[j][c] * w[c]; }
;             lg[e] = a; }
	v_pk_fma_f32 v[178:179], v[68:69], v[244:245], v[178:179] op_sel_hi:[1,0,1]
	s_nop 0
	v_pk_fma_f32 v[174:175], v[70:71], v[244:245], v[178:179] op_sel:[0,1,0]
	s_nop 0
	v_pk_fma_f32 v[174:175], v[72:73], v[246:247], v[174:175] op_sel_hi:[1,0,1]
	v_mov_b32_e32 v176, v247
	v_pk_fma_f32 v[174:175], v[74:75], v[176:177], v[174:175] op_sel_hi:[1,0,1]
	ds_read_b128 v[240:243], v202 offset:36864
	s_waitcnt lgkmcnt(4)
	v_pk_fma_f32 v[180:181], v[124:125], v[224:225], 0 op_sel_hi:[1,0,0]
	s_nop 0
	v_pk_fma_f32 v[176:177], v[126:127], v[224:225], v[180:181] op_sel:[0,1,0]
	s_nop 0
	v_pk_fma_f32 v[176:177], v[128:129], v[226:227], v[176:177] op_sel_hi:[1,0,1]
	v_mov_b32_e32 v178, v227
	v_pk_fma_f32 v[180:181], v[130:131], v[178:179], v[176:177] op_sel_hi:[1,0,1]
	ds_read_b128 v[244:247], v202 offset:37888
	s_waitcnt lgkmcnt(4)
	v_pk_fma_f32 v[180:181], v[112:113], v[228:229], v[180:181] op_sel_hi:[1,0,1]
	s_nop 0
	v_pk_fma_f32 v[176:177], v[114:115], v[228:229], v[180:181] op_sel:[0,1,0]
	s_nop 0
	v_pk_fma_f32 v[176:177], v[118:119], v[230:231], v[176:177] op_sel_hi:[1,0,1]
	v_mov_b32_e32 v178, v231
	v_pk_fma_f32 v[180:181], v[122:123], v[178:179], v[176:177] op_sel_hi:[1,0,1]
	ds_read_b128 v[224:227], v202 offset:38912
	s_waitcnt lgkmcnt(4)
	v_pk_fma_f32 v[180:181], v[108:109], v[232:233], v[180:181] op_sel_hi:[1,0,1]
	s_nop 0
	v_pk_fma_f32 v[176:177], v[110:111], v[232:233], v[180:181] op_sel:[0,1,0]
	s_nop 0
	v_pk_fma_f32 v[176:177], v[116:117], v[234:235], v[176:177] op_sel_hi:[1,0,1]
	v_mov_b32_e32 v178, v235
	v_pk_fma_f32 v[180:181], v[120:121], v[178:179], v[176:177] op_sel_hi:[1,0,1]
	ds_read_b128 v[228:231], v202 offset:39936
	s_waitcnt lgkmcnt(4)
	v_pk_fma_f32 v[180:181], v[96:97], v[236:237], v[180:181] op_sel_hi:[1,0,1]
	s_nop 0
	v_pk_fma_f32 v[176:177], v[98:99], v[236:237], v[180:181] op_sel:[0,1,0]
	s_nop 0
	v_pk_fma_f32 v[176:177], v[102:103], v[238:239], v[176:177] op_sel_hi:[1,0,1]
	v_mov_b32_e32 v178, v239
	v_pk_fma_f32 v[180:181], v[106:107], v[178:179], v[176:177] op_sel_hi:[1,0,1]
	ds_read_b128 v[232:235], v202 offset:40960
	s_waitcnt lgkmcnt(4)
	v_pk_fma_f32 v[180:181], v[92:93], v[240:241], v[180:181] op_sel_hi:[1,0,1]
	s_nop 0
	v_pk_fma_f32 v[176:177], v[94:95], v[240:241], v[180:181] op_sel:[0,1,0]
	s_nop 0
	v_pk_fma_f32 v[176:177], v[100:101], v[242:243], v[176:177] op_sel_hi:[1,0,1]
	v_mov_b32_e32 v178, v243
	v_pk_fma_f32 v[180:181], v[104:105], v[178:179], v[176:177] op_sel_hi:[1,0,1]
	ds_read_b128 v[236:239], v202 offset:41984
	s_waitcnt lgkmcnt(4)
	v_pk_fma_f32 v[180:181], v[80:81], v[244:245], v[180:181] op_sel_hi:[1,0,1]
	s_nop 0
	v_pk_fma_f32 v[176:177], v[82:83], v[244:245], v[180:181] op_sel:[0,1,0]
	s_nop 0
	v_pk_fma_f32 v[176:177], v[86:87], v[246:247], v[176:177] op_sel_hi:[1,0,1]
	v_mov_b32_e32 v178, v247
	v_pk_fma_f32 v[180:181], v[90:91], v[178:179], v[176:177] op_sel_hi:[1,0,1]
	ds_read_b128 v[240:243], v202 offset:43008
	s_waitcnt lgkmcnt(4)
	v_pk_fma_f32 v[180:181], v[76:77], v[224:225], v[180:181] op_sel_hi:[1,0,1]
	s_nop 0
	v_pk_fma_f32 v[176:177], v[78:79], v[224:225], v[180:181] op_sel:[0,1,0]
	s_nop 0
	v_pk_fma_f32 v[176:177], v[84:85], v[226:227], v[176:177] op_sel_hi:[1,0,1]
	v_mov_b32_e32 v178, v227
	v_pk_fma_f32 v[180:181], v[88:89], v[178:179], v[176:177] op_sel_hi:[1,0,1]
	ds_read_b128 v[244:247], v202 offset:44032
	s_waitcnt lgkmcnt(4)
	v_pk_fma_f32 v[180:181], v[68:69], v[228:229], v[180:181] op_sel_hi:[1,0,1]
	s_nop 0
	v_pk_fma_f32 v[176:177], v[70:71], v[228:229], v[180:181] op_sel:[0,1,0]
	s_nop 0
	v_pk_fma_f32 v[176:177], v[72:73], v[230:231], v[176:177] op_sel_hi:[1,0,1]
	v_mov_b32_e32 v178, v231
	v_pk_fma_f32 v[176:177], v[74:75], v[178:179], v[176:177] op_sel_hi:[1,0,1]
	ds_read_b128 v[224:227], v202 offset:45056
	s_waitcnt lgkmcnt(4)
	v_pk_fma_f32 v[184:185], v[124:125], v[232:233], 0 op_sel_hi:[1,0,0]
	s_nop 0
	v_pk_fma_f32 v[178:179], v[126:127], v[232:233], v[184:185] op_sel:[0,1,0]
	s_nop 0
	v_pk_fma_f32 v[178:179], v[128:129], v[234:235], v[178:179] op_sel_hi:[1,0,1]
	v_mov_b32_e32 v180, v235
	v_pk_fma_f32 v[184:185], v[130:131], v[180:181], v[178:179] op_sel_hi:[1,0,1]
	ds_read_b128 v[228:231], v202 offset:46080
	s_waitcnt lgkmcnt(4)
	v_pk_fma_f32 v[184:185], v[112:113], v[236:237], v[184:185] op_sel_hi:[1,0,1]
	s_nop 0
	v_pk_fma_f32 v[178:179], v[114:115], v[236:237], v[184:185] op_sel:[0,1,0]
	s_nop 0
	v_pk_fma_f32 v[178:179], v[118:119], v[238:239], v[178:179] op_sel_hi:[1,0,1]
	v_mov_b32_e32 v180, v239
	v_pk_fma_f32 v[184:185], v[122:123], v[180:181], v[178:179] op_sel_hi:[1,0,1]
	ds_read_b128 v[232:235], v202 offset:47104
	s_waitcnt lgkmcnt(4)
	v_pk_fma_f32 v[184:185], v[108:109], v[240:241], v[184:185] op_sel_hi:[1,0,1]
	s_nop 0
	v_pk_fma_f32 v[178:179], v[110:111], v[240:241], v[184:185] op_sel:[0,1,0]
	s_nop 0
	v_pk_fma_f32 v[178:179], v[116:117], v[242:243], v[178:179] op_sel_hi:[1,0,1]
	v_mov_b32_e32 v180, v243
	v_pk_fma_f32 v[184:185], v[120:121], v[180:181], v[178:179] op_sel_hi:[1,0,1]
	ds_read_b128 v[236:239], v202 offset:48128
	s_waitcnt lgkmcnt(4)
	v_pk_fma_f32 v[184:185], v[96:97], v[244:245], v[184:185] op_sel_hi:[1,0,1]
	s_nop 0
	v_pk_fma_f32 v[178:179], v[98:99], v[244:245], v[184:185] op_sel:[0,1,0]
	s_nop 0
	v_pk_fma_f32 v[178:179], v[102:103], v[246:247], v[178:179] op_sel_hi:[1,0,1]
	v_mov_b32_e32 v180, v247
	v_pk_fma_f32 v[184:185], v[106:107], v[180:181], v[178:179] op_sel_hi:[1,0,1]
	ds_read_b128 v[240:243], v202 offset:49152
	s_waitcnt lgkmcnt(4)
; #define LAS __attribute__((address_space(3)))
; __device__ __forceinline__ void phase_norm2(const Params& p, const Ctx& F, const int l) {
;     ...
; #pragma unroll
;         for (int e = 0; e < 16; ++e) { f32x2 a = {0.f, 0.f};
; #pragma unroll
;             for (int j = 0; j < 8; ++j) { const f32x4 w = *((const LAS f32x4*)(wr2 + e * DM) + F.lane + 64 * j);
; #pragma unroll
;                 for (int c = 0; c < 4; ++c) a += vv[j][c] * w[c]; }
;             lg[e] = a; }
	v_pk_fma_f32 v[184:185], v[92:93], v[224:225], v[184:185] op_sel_hi:[1,0,1]
	s_nop 0
	v_pk_fma_f32 v[178:179], v[94:95], v[224:225], v[184:185] op_sel:[0,1,0]
	s_nop 0
	v_pk_fma_f32 v[178:179], v[100:101], v[226:227], v[178:179] op_sel_hi:[1,0,1]
	v_mov_b32_e32 v180, v227
	v_pk_fma_f32 v[184:185], v[104:105], v[180:181], v[178:179] op_sel_hi:[1,0,1]
	ds_read_b128 v[244:247], v202 offset:50176
	s_waitcnt lgkmcnt(4)
	v_pk_fma_f32 v[184:185], v[80:81], v[228:229], v[184:185] op_sel_hi:[1,0,1]
	s_nop 0
	v_pk_fma_f32 v[178:179], v[82:83], v[228:229], v[184:185] op_sel:[0,1,0]
	s_nop 0
	v_pk_fma_f32 v[178:179], v[86:87], v[230:231], v[178:179] op_sel_hi:[1,0,1]
	v_mov_b32_e32 v180, v231
	v_pk_fma_f32 v[184:185], v[90:91], v[180:181], v[178:179] op_sel_hi:[1,0,1]
	ds_read_b128 v[224:227], v202 offset:51200
	s_waitcnt lgkmcnt(4)
	v_pk_fma_f32 v[184:185], v[76:77], v[232:233], v[184:185] op_sel_hi:[1,0,1]
	s_nop 0
	v_pk_fma_f32 v[178:179], v[78:79], v[232:233], v[184:185] op_sel:[0,1,0]
	s_nop 0
	v_pk_fma_f32 v[178:179], v[84:85], v[234:235], v[178:179] op_sel_hi:[1,0,1]
	v_mov_b32_e32 v180, v235
	v_pk_fma_f32 v[184:185], v[88:89], v[180:181], v[178:179] op_sel_hi:[1,0,1]
	ds_read_b128 v[228:231], v202 offset:52224
	s_waitcnt lgkmcnt(4)
	v_pk_fma_f32 v[184:185], v[68:69], v[236:237], v[184:185] op_sel_hi:[1,0,1]
	s_nop 0
	v_pk_fma_f32 v[178:179], v[70:71], v[236:237], v[184:185] op_sel:[0,1,0]
	ds_read_b128 v[232:235], v202 offset:53248
	v_pk_fma_f32 v[178:179], v[72:73], v[238:239], v[178:179] op_sel_hi:[1,0,1]
	v_mov_b32_e32 v180, v239
	v_pk_fma_f32 v[178:179], v[74:75], v[180:181], v[178:179] op_sel_hi:[1,0,1]
	s_waitcnt lgkmcnt(4)
	v_pk_fma_f32 v[180:181], v[124:125], v[240:241], 0 op_sel_hi:[1,0,0]
	s_nop 0
	v_pk_fma_f32 v[180:181], v[126:127], v[240:241], v[180:181] op_sel:[0,1,0]
	v_mov_b32_e32 v184, v243
	v_pk_fma_f32 v[180:181], v[128:129], v[242:243], v[180:181] op_sel_hi:[1,0,1]
	s_nop 0
	v_pk_fma_f32 v[180:181], v[130:131], v[184:185], v[180:181] op_sel_hi:[1,0,1]
	ds_read_b128 v[236:239], v202 offset:54272
	s_waitcnt lgkmcnt(4)
	v_pk_fma_f32 v[180:181], v[112:113], v[244:245], v[180:181] op_sel_hi:[1,0,1]
	s_nop 0
	v_pk_fma_f32 v[180:181], v[114:115], v[244:245], v[180:181] op_sel:[0,1,0]
	v_mov_b32_e32 v184, v247
	v_pk_fma_f32 v[180:181], v[118:119], v[246:247], v[180:181] op_sel_hi:[1,0,1]
	s_nop 0
	v_pk_fma_f32 v[180:181], v[122:123], v[184:185], v[180:181] op_sel_hi:[1,0,1]
	ds_read_b128 v[240:243], v202 offset:55296
	s_waitcnt lgkmcnt(4)
	v_pk_fma_f32 v[180:181], v[108:109], v[224:225], v[180:181] op_sel_hi:[1,0,1]
	s_nop 0
	v_pk_fma_f32 v[180:181], v[110:111], v[224:225], v[180:181] op_sel:[0,1,0]
	v_mov_b32_e32 v184, v227
	v_pk_fma_f32 v[180:181], v[116:117], v[226:227], v[180:181] op_sel_hi:[1,0,1]
	s_nop 0
	v_pk_fma_f32 v[180:181], v[120:121], v[184:185], v[180:181] op_sel_hi:[1,0,1]
	ds_read_b128 v[244:247], v202 offset:56320
	s_waitcnt lgkmcnt(4)
	v_pk_fma_f32 v[180:181], v[96:97], v[228:229], v[180:181] op_sel_hi:[1,0,1]
	s_nop 0
	v_pk_fma_f32 v[180:181], v[98:99], v[228:229], v[180:181] op_sel:[0,1,0]
	v_mov_b32_e32 v184, v231
	v_pk_fma_f32 v[180:181], v[102:103], v[230:231], v[180:181] op_sel_hi:[1,0,1]
	s_nop 0
	v_pk_fma_f32 v[180:181], v[106:107], v[184:185], v[180:181] op_sel_hi:[1,0,1]
	ds_read_b128 v[224:227], v202 offset:57344
	s_waitcnt lgkmcnt(4)
	v_pk_fma_f32 v[180:181], v[92:93], v[232:233], v[180:181] op_sel_hi:[1,0,1]
	s_nop 0
	v_pk_fma_f32 v[180:181], v[94:95], v[232:233], v[180:181] op_sel:[0,1,0]
	v_mov_b32_e32 v184, v235
	v_pk_fma_f32 v[180:181], v[100:101], v[234:235], v[180:181] op_sel_hi:[1,0,1]
	s_nop 0
	v_pk_fma_f32 v[180:181], v[104:105], v[184:185], v[180:181] op_sel_hi:[1,0,1]
	ds_read_b128 v[228:231], v202 offset:58368
	s_waitcnt lgkmcnt(4)
	v_pk_fma_f32 v[180:181], v[80:81], v[236:237], v[180:181] op_sel_hi:[1,0,1]
	s_nop 0
	v_pk_fma_f32 v[180:181], v[82:83], v[236:237], v[180:181] op_sel:[0,1,0]
	v_mov_b32_e32 v184, v239
	v_pk_fma_f32 v[180:181], v[86:87], v[238:239], v[180:181] op_sel_hi:[1,0,1]
	s_nop 0
	v_pk_fma_f32 v[180:181], v[90:91], v[184:185], v[180:181] op_sel_hi:[1,0,1]
	ds_read_b128 v[232:235], v202 offset:59392
	s_waitcnt lgkmcnt(4)
	v_pk_fma_f32 v[180:181], v[76:77], v[240:241], v[180:181] op_sel_hi:[1,0,1]
	s_nop 0
	v_pk_fma_f32 v[180:181], v[78:79], v[240:241], v[180:181] op_sel:[0,1,0]
	v_mov_b32_e32 v184, v243
	v_pk_fma_f32 v[180:181], v[84:85], v[242:243], v[180:181] op_sel_hi:[1,0,1]
	s_nop 0
	v_pk_fma_f32 v[180:181], v[88:89], v[184:185], v[180:181] op_sel_hi:[1,0,1]
	ds_read_b128 v[236:239], v202 offset:60416
	s_waitcnt lgkmcnt(4)
	v_pk_fma_f32 v[180:181], v[68:69], v[244:245], v[180:181] op_sel_hi:[1,0,1]
	s_nop 0
	v_pk_fma_f32 v[180:181], v[70:71], v[244:245], v[180:181] op_sel:[0,1,0]
	v_mov_b32_e32 v184, v247
	v_pk_fma_f32 v[180:181], v[72:73], v[246:247], v[180:181] op_sel_hi:[1,0,1]
	s_nop 0
	v_pk_fma_f32 v[180:181], v[74:75], v[184:185], v[180:181] op_sel_hi:[1,0,1]
	ds_read_b128 v[240:243], v202 offset:61440
	s_waitcnt lgkmcnt(4)
	v_pk_fma_f32 v[124:125], v[124:125], v[224:225], 0 op_sel_hi:[1,0,0]
	s_nop 0
	v_pk_fma_f32 v[124:125], v[126:127], v[224:225], v[124:125] op_sel:[0,1,0]
	v_mov_b32_e32 v126, v227
	v_pk_fma_f32 v[124:125], v[128:129], v[226:227], v[124:125] op_sel_hi:[1,0,1]
	s_nop 0
	v_pk_fma_f32 v[128:129], v[130:131], v[126:127], v[124:125] op_sel_hi:[1,0,1]
	ds_read_b128 v[244:247], v202 offset:62464
	s_waitcnt lgkmcnt(4)
	v_pk_fma_f32 v[112:113], v[112:113], v[228:229], v[128:129] op_sel_hi:[1,0,1]
	s_nop 0
	v_pk_fma_f32 v[112:113], v[114:115], v[228:229], v[112:113] op_sel:[0,1,0]
	v_mov_b32_e32 v114, v231
	v_pk_fma_f32 v[112:113], v[118:119], v[230:231], v[112:113] op_sel_hi:[1,0,1]
	s_nop 0
	v_pk_fma_f32 v[118:119], v[122:123], v[114:115], v[112:113] op_sel_hi:[1,0,1]
	ds_read_b128 v[224:227], v202 offset:63488
	s_waitcnt lgkmcnt(4)
; #define LAS __attribute__((address_space(3)))
; __device__ __forceinline__ void router_tail(const Ctx& F, const float (&lg)[16], const int b, const int t, const bool valid) {
;     const bool b5 = (F.lane & 32) != 0, b4 = (F.lane & 16) != 0, b3 = (F.lane & 8) != 0, b2 = (F.lane & 4) != 0;
;     float r8[8], r4[4], r2[2];
; #pragma unroll
;     for (int e = 0; e < 8; ++e) { const float keep = b5 ? lg[e + 8] : lg[e], send = b5 ? lg[e] : lg[e + 8]; r8[e] = keep + __shfl_xor(send, 32); }
; #pragma unroll
;     for (int e = 0; e < 4; ++e) { const float keep = b4 ? r8[e + 4] : r8[e], send = b4 ? r8[e] : r8[e + 4]; r4[e] = keep + __shfl_xor(send, 16); }
; #pragma unroll
;     for (int e = 0; e < 2; ++e) { const float keep = b3 ? r4[e + 2] : r4[e], send = b3 ? r4[e] : r4[e + 2]; r2[e] = keep + __shfl_xor(send, 8); }
;     float lgt; { const float keep = b2 ? r2[1] : r2[0], send = b2 ? r2[0] : r2[1]; lgt = keep + __shfl_xor(send, 4); }
;     lgt += __shfl_xor(lgt, 2); lgt += __shfl_xor(lgt, 1);
;     float mx = lgt;
;     mx = fmaxf(mx, __shfl_xor(mx, 4)); mx = fmaxf(mx, __shfl_xor(mx, 8)); mx = fmaxf(mx, __shfl_xor(mx, 16)); mx = fmaxf(mx, __shfl_xor(mx, 32));
;     const float ex = expf(lgt - mx); float sum = ex;
;     sum += __shfl_xor(sum, 4); sum += __shfl_xor(sum, 8); sum += __shfl_xor(sum, 16); sum += __shfl_xor(sum, 32);
;     if (valid && (F.lane & 3) == 0) { const float af = ex / sum; const int e = F.lane >> 2;
; __device__ __forceinline__ void phase_norm2(const Params& p, const Ctx& F, const int l) {
;     ...
;         for (int e = 0; e < 16; ++e) { f32x2 a = {0.f, 0.f};
; #pragma unroll
;             for (int j = 0; j < 8; ++j) { const f32x4 w = *((const LAS f32x4*)(wr2 + e * DM) + F.lane + 64 * j);
; #pragma unroll
;                 for (int c = 0; c < 4; ++c) a += vv[j][c] * w[c]; }
;             lg[e] = a; }
;         float lg0[16], lg1[16];
; #pragma unroll
;         for (int e = 0; e < 16; ++e) { lg0[e] = lg[e].x; lg1[e] = lg[e].y; }
	v_pk_fma_f32 v[108:109], v[108:109], v[232:233], v[118:119] op_sel_hi:[1,0,1]
	s_nop 0
	v_pk_fma_f32 v[108:109], v[110:111], v[232:233], v[108:109] op_sel:[0,1,0]
	v_mov_b32_e32 v110, v235
	v_pk_fma_f32 v[108:109], v[116:117], v[234:235], v[108:109] op_sel_hi:[1,0,1]
	s_nop 0
	v_pk_fma_f32 v[112:113], v[120:121], v[110:111], v[108:109] op_sel_hi:[1,0,1]
	ds_read_b128 v[228:231], v202 offset:64512
	s_waitcnt lgkmcnt(4)
	v_pk_fma_f32 v[96:97], v[96:97], v[236:237], v[112:113] op_sel_hi:[1,0,1]
	s_nop 0
	v_pk_fma_f32 v[96:97], v[98:99], v[236:237], v[96:97] op_sel:[0,1,0]
	v_mov_b32_e32 v98, v239
	v_pk_fma_f32 v[96:97], v[102:103], v[238:239], v[96:97] op_sel_hi:[1,0,1]
	s_nop 0
	v_pk_fma_f32 v[102:103], v[106:107], v[98:99], v[96:97] op_sel_hi:[1,0,1]
	s_waitcnt lgkmcnt(3)
	v_pk_fma_f32 v[92:93], v[92:93], v[240:241], v[102:103] op_sel_hi:[1,0,1]
	s_nop 0
	v_pk_fma_f32 v[92:93], v[94:95], v[240:241], v[92:93] op_sel:[0,1,0]
	v_mov_b32_e32 v94, v243
	v_pk_fma_f32 v[92:93], v[100:101], v[242:243], v[92:93] op_sel_hi:[1,0,1]
	s_nop 0
	v_pk_fma_f32 v[96:97], v[104:105], v[94:95], v[92:93] op_sel_hi:[1,0,1]
	s_waitcnt lgkmcnt(2)
	v_pk_fma_f32 v[80:81], v[80:81], v[244:245], v[96:97] op_sel_hi:[1,0,1]
	s_nop 0
	v_pk_fma_f32 v[80:81], v[82:83], v[244:245], v[80:81] op_sel:[0,1,0]
	v_mov_b32_e32 v82, v247
	v_pk_fma_f32 v[80:81], v[86:87], v[246:247], v[80:81] op_sel_hi:[1,0,1]
	s_nop 0
	v_pk_fma_f32 v[86:87], v[90:91], v[82:83], v[80:81] op_sel_hi:[1,0,1]
	s_waitcnt lgkmcnt(1)
	v_pk_fma_f32 v[76:77], v[76:77], v[224:225], v[86:87] op_sel_hi:[1,0,1]
	s_nop 0
	v_pk_fma_f32 v[76:77], v[78:79], v[224:225], v[76:77] op_sel:[0,1,0]
	v_mov_b32_e32 v78, v227
	v_pk_fma_f32 v[76:77], v[84:85], v[226:227], v[76:77] op_sel_hi:[1,0,1]
	s_nop 0
	v_pk_fma_f32 v[80:81], v[88:89], v[78:79], v[76:77] op_sel_hi:[1,0,1]
	v_cndmask_b32_e64 v1, v168, v152, s[38:39]
	s_waitcnt lgkmcnt(0)
	v_pk_fma_f32 v[68:69], v[68:69], v[228:229], v[80:81] op_sel_hi:[1,0,1]
	s_nop 0
	v_pk_fma_f32 v[68:69], v[70:71], v[228:229], v[68:69] op_sel:[0,1,0]
	v_mov_b32_e32 v70, v231
	v_pk_fma_f32 v[68:69], v[72:73], v[230:231], v[68:69] op_sel_hi:[1,0,1]
	v_cndmask_b32_e64 v72, v156, v172, s[38:39]
	v_pk_fma_f32 v[68:69], v[74:75], v[70:71], v[68:69] op_sel_hi:[1,0,1]
	s_nop 1
	v_permlane32_swap_b32_e32 v152, v168
	v_permlane32_swap_b32_e32 v154, v170
	v_permlane32_swap_b32_e32 v156, v172
	v_permlane32_swap_b32_e32 v158, v174
	v_permlane32_swap_b32_e32 v160, v176
	v_permlane32_swap_b32_e32 v162, v178
	v_permlane32_swap_b32_e32 v164, v180
	v_permlane32_swap_b32_e32 v166, v68
	v_add_f32_e32 v1, v152, v168
	v_add_f32_e32 v70, v154, v170
	v_add_f32_e32 v71, v156, v172
	v_add_f32_e32 v72, v158, v174
	v_add_f32_e32 v73, v160, v176
	v_add_f32_e32 v74, v162, v178
	v_add_f32_e32 v75, v164, v180
	v_add_f32_e32 v68, v166, v68
	s_waitcnt lgkmcnt(0)
	v_cndmask_b32_e64 v76, v73, v1, s[40:41]
	v_cndmask_b32_e64 v1, v1, v73, s[40:41]
	v_cndmask_b32_e64 v73, v74, v70, s[40:41]
	v_cndmask_b32_e64 v70, v70, v74, s[40:41]
	ds_bpermute_b32 v70, v193, v70
	ds_bpermute_b32 v1, v193, v1
	s_waitcnt lgkmcnt(1)
	v_add_f32_e32 v70, v73, v70
	v_cndmask_b32_e64 v73, v75, v71, s[40:41]
	v_cndmask_b32_e64 v71, v71, v75, s[40:41]
	ds_bpermute_b32 v71, v193, v71
	s_waitcnt lgkmcnt(1)
	v_add_f32_e32 v1, v76, v1
	s_waitcnt lgkmcnt(0)
	v_add_f32_e32 v71, v73, v71
	v_cndmask_b32_e64 v73, v68, v72, s[40:41]
	v_cndmask_b32_e64 v68, v72, v68, s[40:41]
	ds_bpermute_b32 v68, v193, v68
	v_cndmask_b32_e64 v72, v71, v1, s[42:43]
	v_cndmask_b32_e64 v1, v1, v71, s[42:43]
	ds_bpermute_b32 v1, v192, v1
	s_waitcnt lgkmcnt(1)
	v_add_f32_e32 v68, v73, v68
	v_cndmask_b32_e64 v71, v68, v70, s[42:43]
	v_cndmask_b32_e64 v68, v70, v68, s[42:43]
	ds_bpermute_b32 v68, v192, v68
	s_waitcnt lgkmcnt(1)
	v_add_f32_e32 v1, v72, v1
	s_waitcnt lgkmcnt(0)
	v_add_f32_e32 v68, v71, v68
	v_cndmask_b32_e64 v70, v68, v1, s[4:5]
	v_cndmask_b32_e64 v1, v1, v68, s[4:5]
	ds_bpermute_b32 v1, v191, v1
	s_waitcnt lgkmcnt(0)
	v_add_f32_e32 v1, v70, v1
	s_nop 1
	v_add_f32_dpp v1, v1, v1 quad_perm:[2,3,0,1] row_mask:0xf bank_mask:0xf
	s_nop 1
	v_add_f32_dpp v1, v1, v1 quad_perm:[1,0,3,2] row_mask:0xf bank_mask:0xf
	s_nop 1
	v_max_f32_dpp v68, v1, v1 row_half_mirror row_mask:0xf bank_mask:0xf
	s_nop 1
	v_max_f32_dpp v68, v68, v68 row_mirror row_mask:0xf bank_mask:0xf
	v_mov_b32_e32 v70, v68
	s_nop 1
	v_permlane16_swap_b32_e32 v68, v70
	v_max_f32_e32 v68, v68, v70
	v_mov_b32_e32 v70, v68
	s_nop 1
	v_permlane32_swap_b32_e32 v68, v70
	v_max_f32_e32 v68, v68, v70
	v_sub_f32_e32 v1, v1, v68
	v_mul_f32_e32 v68, 0x3fb8aa3b, v1
	v_fma_f32 v70, v1, s55, -v68
	v_rndne_f32_e32 v71, v68
	v_fmac_f32_e32 v70, 0x32a5705f, v1
	v_sub_f32_e32 v68, v68, v71
	v_add_f32_e32 v68, v68, v70
	v_exp_f32_e32 v68, v68
	v_cvt_i32_f32_e32 v70, v71
	v_cmp_ngt_f32_e32 vcc, s56, v1
	v_ldexp_f32 v68, v68, v70
	s_nop 0
	v_cndmask_b32_e32 v68, 0, v68, vcc
	v_cmp_nlt_f32_e32 vcc, s57, v1
	s_nop 1
	v_cndmask_b32_e32 v68, v222, v68, vcc
	s_nop 1
	v_add_f32_dpp v1, v68, v68 row_half_mirror row_mask:0xf bank_mask:0xf
	s_nop 1
	v_add_f32_dpp v1, v1, v1 row_mirror row_mask:0xf bank_mask:0xf
	v_mov_b32_e32 v70, v1
	s_nop 1
	v_permlane16_swap_b32_e32 v1, v70
	v_add_f32_e32 v70, v1, v70
	ds_bpermute_b32 v71, v194, v70
	s_and_saveexec_b64 s[0:1], s[6:7]
	s_cbranch_execz .LBB0_942
	s_waitcnt lgkmcnt(0)
	v_add_f32_e32 v1, v70, v71
	v_div_scale_f32 v70, s[12:13], v1, v1, v68
	v_rcp_f32_e32 v71, v70
	v_div_scale_f32 v72, vcc, v68, v1, v68
	s_cmpk_gt_i32 s60, 0xff
	v_fma_f32 v73, -v70, v71, 1.0
	v_fmac_f32_e32 v71, v73, v71
	v_mul_f32_e32 v73, v72, v71
	v_fma_f32 v74, -v70, v73, v72
	v_fmac_f32_e32 v73, v74, v71
	v_fma_f32 v70, -v70, v73, v72
	v_div_fmas_f32 v70, v70, v71, v73
	v_div_fixup_f32 v68, v70, v1, v68
	s_mov_b64 s[12:13], -1
	s_cbranch_scc0 .LBB0_940
	v_lshl_add_u64 v[70:71], s[60:61], 2, v[148:149]
	global_store_dword v[70:71], v68, off offset:-1024
	s_mov_b64 s[12:13], 0
